# v96 + nt on the retention phase's y stores (138 MB written while q/k rows are shared through L2 by the 8 slice workgroups of each (b,head))
# speedup vs baseline: 1.0114x; 1.0047x over previous
.LBB0_267:
	s_add_u32 s56, s76, 0x80
	s_nop 10
	v_cndmask_b32_e64 v0, v62, v78, s[0:1]
	v_cndmask_b32_e64 v9, v63, v79, s[0:1]
	v_cndmask_b32_e64 v8, v60, v76, s[0:1]
	v_cndmask_b32_e64 v7, v58, v74, s[0:1]
	v_cndmask_b32_e64 v6, v56, v72, s[0:1]
	v_cndmask_b32_e64 v5, v54, v70, s[0:1]
	v_cndmask_b32_e64 v4, v52, v68, s[0:1]
	v_cndmask_b32_e64 v3, v50, v66, s[0:1]
	v_cndmask_b32_e64 v2, v48, v64, s[0:1]
	s_addc_u32 s57, s77, 0
	v_cndmask_b32_e64 v10, v61, v77, s[0:1]
	v_cndmask_b32_e64 v11, v59, v75, s[0:1]
	v_cndmask_b32_e64 v12, v57, v73, s[0:1]
	v_cndmask_b32_e64 v13, v55, v71, s[0:1]
	v_cndmask_b32_e64 v14, v53, v69, s[0:1]
	v_cndmask_b32_e64 v15, v51, v67, s[0:1]
	v_cndmask_b32_e64 v80, v49, v65, s[0:1]
	v_cvt_pk_bf16_f32 v2, v2, v80
	v_cvt_pk_bf16_f32 v3, v3, v15
	v_cvt_pk_bf16_f32 v4, v4, v14
	v_cvt_pk_bf16_f32 v5, v5, v13
	v_cvt_pk_bf16_f32 v6, v6, v12
	v_cvt_pk_bf16_f32 v7, v7, v11
	v_cvt_pk_bf16_f32 v8, v8, v10
	v_cvt_pk_bf16_f32 v9, v0, v9
	v_add_u32_e32 v0, s81, v171
	s_cmp_eq_u32 s84, 0x2000000
	ds_write_b128 v0, v[2:5]
	ds_write_b128 v0, v[6:9] offset:16
	s_cselect_b32 s77, s77, s57
	s_cselect_b32 s76, s76, s56
	v_mov_b32_e32 v2, v169
	s_lshl_b64 s[54:55], s[76:77], 12
	s_add_u32 vcc_lo, s58, s54
	v_lshlrev_b32_e32 v3, 4, v2
	v_lshlrev_b32_e32 v0, 7, v2
	v_and_b32_e32 v4, 0x1f0, v3
	s_addc_u32 vcc_hi, s59, s55
	v_and_or_b32 v0, v0, s39, v4
	v_lshl_add_u64 v[14:15], vcc, 0, v[0:1]
	v_lshlrev_b32_e32 v198, 10, v2
	v_and_b32_e32 v199, 0x70, v3
	global_load_dwordx4 v[2:5], v0, vcc
	v_add_co_u32_e32 v6, vcc, s33, v14
	s_lshl_b64 s[54:55], s[76:77], 13
	s_nop 0
	v_addc_co_u32_e32 v7, vcc, 0, v15, vcc
	v_add_co_u32_e32 v10, vcc, s40, v14
	s_add_u32 s54, s36, s54
	s_nop 0
	v_addc_co_u32_e32 v11, vcc, 0, v15, vcc
	v_add_co_u32_e32 v80, vcc, s41, v14
	s_addc_u32 s55, s37, s55
	s_nop 0
	v_addc_co_u32_e32 v81, vcc, 0, v15, vcc
	v_add_co_u32_e32 v84, vcc, s42, v14
	v_and_or_b32 v0, v198, s48, v199
	s_nop 0
	v_addc_co_u32_e32 v85, vcc, 0, v15, vcc
	v_add_co_u32_e32 v88, vcc, s43, v14
	v_or_b32_e32 v197, s79, v160
	s_nop 0
	v_addc_co_u32_e32 v89, vcc, 0, v15, vcc
	v_add_co_u32_e32 v92, vcc, s44, v14
	global_load_dwordx4 v[10:13], v[10:11], off
	s_nop 0
	v_addc_co_u32_e32 v93, vcc, 0, v15, vcc
	v_add_co_u32_e32 v14, vcc, s45, v14
	global_load_dwordx4 v[6:9], v[6:7], off
	s_nop 0
	v_addc_co_u32_e32 v15, vcc, 0, v15, vcc
	global_load_dwordx4 v[160:163], v[14:15], off
	v_lshl_add_u64 v[14:15], s[54:55], 0, v[0:1]
	v_add_co_u32_e32 v14, vcc, s49, v14
	global_load_dwordx4 v[80:83], v[80:81], off
	s_nop 0
	v_addc_co_u32_e32 v15, vcc, 0, v15, vcc
	global_load_dwordx4 v[84:87], v[84:85], off
	v_cndmask_b32_e64 v55, v71, v55, s[0:1]
	global_load_dwordx4 v[88:91], v[88:89], off
	v_cndmask_b32_e64 v54, v70, v54, s[0:1]
	global_load_dwordx4 v[92:95], v[92:93], off
	v_cndmask_b32_e64 v53, v69, v53, s[0:1]
	v_cndmask_b32_e64 v52, v68, v52, s[0:1]
	v_cndmask_b32_e64 v51, v67, v51, s[0:1]
	v_cndmask_b32_e64 v50, v66, v50, s[0:1]
	v_cndmask_b32_e64 v49, v65, v49, s[0:1]
	v_cndmask_b32_e64 v48, v64, v48, s[0:1]
	global_load_dwordx4 v[64:67], v0, s[54:55]
	global_load_dwordx4 v[68:71], v[14:15], off
	s_add_u32 s54, s76, s62
	s_addc_u32 s55, s77, 0
	s_lshr_b64 s[54:55], s[54:55], 2
	s_add_u32 s54, s54, s47
	s_addc_u32 s55, s55, 0
	s_lshl_b64 s[54:55], s[54:55], 14
	v_readlane_b32 s52, v250, 46
	v_or_b32_e32 v207, v195, v196
	v_readlane_b32 s53, v250, 47
	s_add_u32 s76, s52, s54
	v_bitop3_b32 v0, v197, v165, v194 bitop3:0x36
	s_addc_u32 s77, s53, s55
	v_lshl_or_b32 v0, v0, 4, v207
	s_add_i32 s54, 0, 0x18000
	v_add_u32_e32 v14, s54, v0
	v_or_b32_e32 v206, v197, v194
	v_cndmask_b32_e64 v63, v79, v63, s[0:1]
	v_cndmask_b32_e64 v62, v78, v62, s[0:1]
	v_cndmask_b32_e64 v61, v77, v61, s[0:1]
	v_cndmask_b32_e64 v60, v76, v60, s[0:1]
	v_cndmask_b32_e64 v59, v75, v59, s[0:1]
	v_cndmask_b32_e64 v58, v74, v58, s[0:1]
	v_cndmask_b32_e64 v57, v73, v57, s[0:1]
	v_cndmask_b32_e64 v56, v72, v56, s[0:1]
	v_xad_u32 v0, v0, 16, s54
	ds_read_b64_tr_b16 v[72:73], v14
	ds_read_b64_tr_b16 v[74:75], v0 offset:1024
	ds_read_b64_tr_b16 v[76:77], v14 offset:4096
	ds_read_b64_tr_b16 v[78:79], v0 offset:5120
	ds_read_b64_tr_b16 v[194:195], v14 offset:8192
	ds_read_b64_tr_b16 v[196:197], v0 offset:9216
	ds_read_b64_tr_b16 v[198:199], v14 offset:12288
	ds_read_b64_tr_b16 v[200:201], v0 offset:13312
	ds_read_b64_tr_b16 v[202:203], v14 offset:16384
	ds_read_b64_tr_b16 v[204:205], v0 offset:17408
	ds_read_b64_tr_b16 v[212:213], v14 offset:20480
	ds_read_b64_tr_b16 v[214:215], v0 offset:21504
	ds_read_b64_tr_b16 v[216:217], v14 offset:24576
	ds_read_b64_tr_b16 v[218:219], v0 offset:25600
	ds_read_b64_tr_b16 v[220:221], v14 offset:28672
	ds_read_b64_tr_b16 v[222:223], v0 offset:29696
	s_waitcnt lgkmcnt(0)
	s_waitcnt vmcnt(25) lgkmcnt(14)
	v_mfma_f32_32x32x16_bf16 v[48:63], v[72:75], v[144:147], v[48:63]
	v_mov_b32_e32 v0, v168
	s_nop 0
	v_lshlrev_b32_e32 v0, 4, v0
	v_lshl_add_u64 v[14:15], s[76:77], 0, v[0:1]
	v_add_co_u32_e32 v14, vcc, s63, v14
	s_waitcnt vmcnt(24) lgkmcnt(12)
	v_mfma_f32_32x32x16_bf16 v[48:63], v[76:79], v[152:155], v[48:63]
	v_addc_co_u32_e32 v15, vcc, 0, v15, vcc
	global_load_dwordx4 v[144:147], v0, s[76:77]
	global_load_dwordx4 v[152:155], v0, s[76:77] offset:1024
	s_waitcnt vmcnt(25) lgkmcnt(10)
	v_mfma_f32_32x32x16_bf16 v[48:63], v[194:197], v[140:143], v[48:63]
	s_waitcnt vmcnt(24) lgkmcnt(8)
	v_mfma_f32_32x32x16_bf16 v[48:63], v[198:201], v[136:139], v[48:63]
	global_load_dwordx4 v[140:143], v0, s[76:77] offset:2048
	global_load_dwordx4 v[136:139], v0, s[76:77] offset:3072
	s_waitcnt vmcnt(25) lgkmcnt(6)
	v_mfma_f32_32x32x16_bf16 v[48:63], v[202:205], v[156:159], v[48:63]
	s_waitcnt vmcnt(24) lgkmcnt(4)
	v_mfma_f32_32x32x16_bf16 v[48:63], v[212:215], v[148:151], v[48:63]
	global_load_dwordx4 v[156:159], v[14:15], off
	global_load_dwordx4 v[148:151], v[14:15], off offset:1024
	s_waitcnt vmcnt(25) lgkmcnt(2)
	v_mfma_f32_32x32x16_bf16 v[48:63], v[216:219], v[132:135], v[48:63]
	global_load_dwordx4 v[132:135], v[14:15], off offset:2048
	global_load_dwordx4 v[72:75], v[14:15], off offset:3072
	s_waitcnt vmcnt(26) lgkmcnt(0)
	v_mfma_f32_32x32x16_bf16 v[48:63], v[220:223], v[128:131], v[48:63]
	v_bitop3_b32 v0, v206, v165, 8 bitop3:0x36
	v_lshl_add_u32 v0, v0, 4, v207
	v_add_u32_e32 v14, s54, v0
	v_xad_u32 v0, v0, 16, s54
	ds_read_b64_tr_b16 v[76:77], v14
	ds_read_b64_tr_b16 v[128:129], v14 offset:4096
	ds_read_b64_tr_b16 v[194:195], v14 offset:8192
	ds_read_b64_tr_b16 v[198:199], v14 offset:12288
	ds_read_b64_tr_b16 v[78:79], v0 offset:1024
	ds_read_b64_tr_b16 v[130:131], v0 offset:5120
	ds_read_b64_tr_b16 v[196:197], v0 offset:9216
	ds_read_b64_tr_b16 v[200:201], v0 offset:13312
	ds_read_b64_tr_b16 v[202:203], v14 offset:16384
	ds_read_b64_tr_b16 v[212:213], v14 offset:20480
	ds_read_b64_tr_b16 v[216:217], v14 offset:24576
	ds_read_b64_tr_b16 v[220:221], v14 offset:28672
	ds_read_b64_tr_b16 v[204:205], v0 offset:17408
	ds_read_b64_tr_b16 v[214:215], v0 offset:21504
	ds_read_b64_tr_b16 v[218:219], v0 offset:25600
	ds_read_b64_tr_b16 v[222:223], v0 offset:29696
	s_waitcnt lgkmcnt(0)
	s_waitcnt vmcnt(25) lgkmcnt(11)
	v_mfma_f32_32x32x16_bf16 v[48:63], v[76:79], v[124:127], v[48:63]
	v_mov_b32_e32 v0, v168
	s_nop 0
	v_lshlrev_b32_e32 v0, 4, v0
	v_lshl_add_u64 v[14:15], s[76:77], 0, v[0:1]
	v_add_co_u32_e32 v76, vcc, s80, v14
	s_waitcnt vmcnt(24) lgkmcnt(10)
	v_mfma_f32_32x32x16_bf16 v[48:63], v[128:131], v[120:123], v[48:63]
	v_addc_co_u32_e32 v77, vcc, 0, v15, vcc
	v_add_co_u32_e32 v14, vcc, s78, v14
	s_nop 1
	v_addc_co_u32_e32 v15, vcc, 0, v15, vcc
	s_waitcnt vmcnt(23) lgkmcnt(9)
	v_mfma_f32_32x32x16_bf16 v[48:63], v[194:197], v[112:115], v[48:63]
	s_waitcnt vmcnt(22) lgkmcnt(8)
	v_mfma_f32_32x32x16_bf16 v[48:63], v[198:201], v[108:111], v[48:63]
	s_waitcnt vmcnt(21) lgkmcnt(3)
	v_mfma_f32_32x32x16_bf16 v[48:63], v[202:205], v[116:119], v[48:63]
	s_waitcnt vmcnt(20) lgkmcnt(2)
	v_mfma_f32_32x32x16_bf16 v[48:63], v[212:215], v[104:107], v[48:63]
	global_load_dwordx4 v[120:123], v[76:77], off offset:1024
	global_load_dwordx4 v[112:115], v[76:77], off offset:2048
	global_load_dwordx4 v[124:127], v[14:15], off offset:-4096
	global_load_dwordx4 v[108:111], v[76:77], off offset:3072
	global_load_dwordx4 v[116:119], v[14:15], off
	global_load_dwordx4 v[104:107], v[14:15], off offset:1024
	s_waitcnt vmcnt(25) lgkmcnt(1)
	v_mfma_f32_32x32x16_bf16 v[48:63], v[216:219], v[100:103], v[48:63]
	global_load_dwordx4 v[100:103], v[14:15], off offset:2048
	global_load_dwordx4 v[76:79], v[14:15], off offset:3072
	s_waitcnt vmcnt(26) lgkmcnt(0)
	v_mfma_f32_32x32x16_bf16 v[48:63], v[220:223], v[96:99], v[48:63]
	v_mov_b32_e32 v0, v168
	v_add_u32_e32 v14, s66, v171
	s_barrier
	ds_read_b128 v[96:99], v14
	ds_read_b128 v[128:131], v14 offset:16
	s_add_u32 s54, s38, s84
	s_addc_u32 s55, s60, s85
	s_waitcnt lgkmcnt(1)
	v_lshlrev_b32_e32 v14, 16, v96
	s_nop 2
	v_add_f32_e32 v14, v48, v14
	s_waitcnt lgkmcnt(0)
	v_lshlrev_b32_e32 v48, 16, v128
	v_add_f32_e32 v56, v56, v48
	v_and_b32_e32 v48, 0xffff0000, v128
	v_and_b32_e32 v15, 0xffff0000, v96
	v_add_f32_e32 v57, v57, v48
	v_lshlrev_b32_e32 v48, 16, v97
	v_add_f32_e32 v15, v49, v15
	v_add_f32_e32 v49, v50, v48
	v_and_b32_e32 v48, 0xffff0000, v97
	v_add_f32_e32 v50, v51, v48
	v_lshlrev_b32_e32 v48, 16, v129
	v_add_f32_e32 v58, v58, v48
	v_and_b32_e32 v48, 0xffff0000, v129
	v_add_f32_e32 v59, v59, v48
	v_lshlrev_b32_e32 v48, 16, v98
	v_add_f32_e32 v51, v52, v48
	v_and_b32_e32 v48, 0xffff0000, v98
	v_add_f32_e32 v52, v53, v48
	v_lshlrev_b32_e32 v48, 16, v130
	v_add_f32_e32 v60, v60, v48
	v_and_b32_e32 v48, 0xffff0000, v130
	v_add_f32_e32 v61, v61, v48
	v_lshlrev_b32_e32 v48, 16, v99
	v_add_f32_e32 v53, v54, v48
	v_and_b32_e32 v48, 0xffff0000, v99
	v_add_f32_e32 v54, v55, v48
	v_lshlrev_b32_e32 v48, 16, v131
	v_add_f32_e32 v55, v62, v48
	v_and_b32_e32 v48, 0xffff0000, v131
	v_add_f32_e32 v62, v63, v48
	v_lshlrev_b32_e32 v48, 13, v0
	v_lshrrev_b32_e32 v0, 1, v0
	v_and_b32_e32 v48, 0x3e000, v48
	v_and_b32_e32 v0, 0x7ffffff0, v0
	v_mul_f32_e32 v14, v193, v14
	v_mul_f32_e32 v15, v193, v15
	v_add_u32_e32 v0, v48, v0
	v_cvt_pk_bf16_f32 v48, v14, v15
	v_mul_f32_e32 v14, v193, v49
	v_mul_f32_e32 v15, v193, v50
	v_cvt_pk_bf16_f32 v49, v14, v15
	v_mul_f32_e32 v14, v193, v51
	v_mul_f32_e32 v15, v193, v52
	v_cvt_pk_bf16_f32 v50, v14, v15
	v_mul_f32_e32 v14, v193, v53
	v_mul_f32_e32 v15, v193, v54
	v_cvt_pk_bf16_f32 v51, v14, v15
	v_mul_f32_e32 v14, v193, v56
	v_mul_f32_e32 v15, v193, v57
	v_cvt_pk_bf16_f32 v52, v14, v15
	v_mul_f32_e32 v14, v193, v58
	v_mul_f32_e32 v15, v193, v59
	v_cvt_pk_bf16_f32 v53, v14, v15
	v_mul_f32_e32 v14, v193, v60
	v_mul_f32_e32 v15, v193, v61
	v_cvt_pk_bf16_f32 v54, v14, v15
	v_mul_f32_e32 v14, v193, v55
	v_mul_f32_e32 v15, v193, v62
	v_cvt_pk_bf16_f32 v55, v14, v15
	v_lshl_add_u64 v[14:15], s[54:55], 0, v[0:1]
	s_mov_b32 s54, 0x2bc00000
	v_add_co_u32_e32 v14, vcc, s54, v14
	v_permlane32_swap_b32_e32 v48, v50
	v_permlane32_swap_b32_e32 v49, v51
	v_addc_co_u32_e32 v15, vcc, 0, v15, vcc
	v_permlane32_swap_b32_e32 v52, v54
	v_permlane32_swap_b32_e32 v53, v55
	v_mov_b32_e32 v0, v168
	global_store_dwordx4 v[14:15], v[48:51], off nt
	global_store_dwordx4 v[14:15], v[52:55], off offset:32 nt
	s_nop 0
	v_lshrrev_b32_e32 v14, 3, v0
	v_and_b32_e32 v14, 2, v14
	v_bfe_u32 v15, v0, 1, 1
	v_and_b32_e32 v49, 12, v0
	v_lshrrev_b32_e32 v50, 4, v0
	v_and_or_b32 v49, v50, 2, v49
	v_or_b32_e32 v50, v14, v15
	v_lshlrev_b32_e32 v48, 6, v0
	v_bitop3_b32 v51, v50, v49, s65 bitop3:0x36
	v_lshlrev_b32_e32 v0, 3, v0
	v_and_b32_e32 v48, 0xfffffb00, v48
	v_lshlrev_b32_e32 v51, 4, v51
	v_and_b32_e32 v0, 8, v0
	v_bitop3_b32 v14, v14, v49, v15 bitop3:0x36
	v_bitop3_b32 v15, v50, v49, 4 bitop3:0x36
	v_or3_b32 v51, v51, v48, v0
	v_lshlrev_b32_e32 v14, 4, v14
	v_lshlrev_b32_e32 v15, 4, v15
	v_or3_b32 v14, v14, v48, v0
	v_or3_b32 v0, v15, v48, v0
	v_add_u32_e32 v15, s64, v51
	v_xad_u32 v165, v51, 16, s64
	v_add_u32_e32 v194, s67, v14
	v_xad_u32 v14, v14, 16, s67
	v_add_u32_e32 v195, s67, v0
	v_xad_u32 v0, v0, 16, s67
	ds_read_b64_tr_b16 v[48:49], v15
	ds_read_b64_tr_b16 v[50:51], v165 offset:1024
	ds_read_b64_tr_b16 v[54:55], v165 offset:5120
	ds_read_b64_tr_b16 v[52:53], v15 offset:4096
	ds_read_b64_tr_b16 v[56:57], v194
	ds_read_b64_tr_b16 v[58:59], v14 offset:1024
	ds_read_b64_tr_b16 v[62:63], v14 offset:5120
	ds_read_b64_tr_b16 v[60:61], v194 offset:4096
	ds_read_b64_tr_b16 v[96:97], v195
	ds_read_b64_tr_b16 v[98:99], v0 offset:1024
	ds_read_b64_tr_b16 v[130:131], v0 offset:5120
	ds_read_b64_tr_b16 v[128:129], v195 offset:4096
	s_waitcnt lgkmcnt(0)
	s_waitcnt lgkmcnt(6)
	v_mfma_f32_32x32x16_bf16 v[16:31], v[56:59], v[48:51], v[16:31]
	s_waitcnt lgkmcnt(2)
	v_mfma_f32_32x32x16_bf16 v[32:47], v[96:99], v[48:51], v[32:47]
	v_mfma_f32_32x32x16_bf16 v[16:31], v[60:63], v[52:55], v[16:31]
	s_waitcnt lgkmcnt(0)
	v_mfma_f32_32x32x16_bf16 v[32:47], v[128:131], v[52:55], v[32:47]
	ds_read_b64_tr_b16 v[48:49], v15 offset:8192
	ds_read_b64_tr_b16 v[50:51], v165 offset:9216
	ds_read_b64_tr_b16 v[54:55], v165 offset:13312
	ds_read_b64_tr_b16 v[52:53], v15 offset:12288
	ds_read_b64_tr_b16 v[56:57], v194 offset:8192
	ds_read_b64_tr_b16 v[58:59], v14 offset:9216
	ds_read_b64_tr_b16 v[62:63], v14 offset:13312
	ds_read_b64_tr_b16 v[60:61], v194 offset:12288
	ds_read_b64_tr_b16 v[96:97], v195 offset:8192
	ds_read_b64_tr_b16 v[98:99], v0 offset:9216
	ds_read_b64_tr_b16 v[130:131], v0 offset:13312
	ds_read_b64_tr_b16 v[128:129], v195 offset:12288
	s_waitcnt lgkmcnt(0)
	s_waitcnt lgkmcnt(6)
	v_mfma_f32_32x32x16_bf16 v[16:31], v[56:59], v[48:51], v[16:31]
	s_waitcnt lgkmcnt(2)
	v_mfma_f32_32x32x16_bf16 v[32:47], v[96:99], v[48:51], v[32:47]
	v_mfma_f32_32x32x16_bf16 v[16:31], v[60:63], v[52:55], v[16:31]
	s_waitcnt lgkmcnt(0)
	v_mfma_f32_32x32x16_bf16 v[32:47], v[128:131], v[52:55], v[32:47]
	ds_read_b64_tr_b16 v[48:49], v15 offset:16384
	ds_read_b64_tr_b16 v[50:51], v165 offset:17408
	ds_read_b64_tr_b16 v[54:55], v165 offset:21504
	ds_read_b64_tr_b16 v[52:53], v15 offset:20480
	ds_read_b64_tr_b16 v[56:57], v194 offset:16384
	ds_read_b64_tr_b16 v[58:59], v14 offset:17408
	ds_read_b64_tr_b16 v[62:63], v14 offset:21504
	ds_read_b64_tr_b16 v[60:61], v194 offset:20480
	ds_read_b64_tr_b16 v[96:97], v195 offset:16384
	ds_read_b64_tr_b16 v[98:99], v0 offset:17408
	ds_read_b64_tr_b16 v[130:131], v0 offset:21504
	ds_read_b64_tr_b16 v[128:129], v195 offset:20480
	s_waitcnt lgkmcnt(0)
	s_waitcnt lgkmcnt(6)
	v_mfma_f32_32x32x16_bf16 v[16:31], v[56:59], v[48:51], v[16:31]
	s_waitcnt lgkmcnt(2)
	v_mfma_f32_32x32x16_bf16 v[32:47], v[96:99], v[48:51], v[32:47]
	v_mfma_f32_32x32x16_bf16 v[16:31], v[60:63], v[52:55], v[16:31]
	s_waitcnt lgkmcnt(0)
	v_mfma_f32_32x32x16_bf16 v[32:47], v[128:131], v[52:55], v[32:47]
	ds_read_b64_tr_b16 v[48:49], v15 offset:24576
	ds_read_b64_tr_b16 v[50:51], v165 offset:25600
	ds_read_b64_tr_b16 v[54:55], v165 offset:29696
	ds_read_b64_tr_b16 v[52:53], v15 offset:28672
	ds_read_b64_tr_b16 v[56:57], v194 offset:24576
	ds_read_b64_tr_b16 v[58:59], v14 offset:25600
	ds_read_b64_tr_b16 v[62:63], v14 offset:29696
	ds_read_b64_tr_b16 v[60:61], v194 offset:28672
	ds_read_b64_tr_b16 v[96:97], v195 offset:24576
	ds_read_b64_tr_b16 v[98:99], v0 offset:25600
	ds_read_b64_tr_b16 v[130:131], v0 offset:29696
	ds_read_b64_tr_b16 v[128:129], v195 offset:28672
	s_waitcnt lgkmcnt(0)
	s_waitcnt lgkmcnt(6)
	v_mfma_f32_32x32x16_bf16 v[16:31], v[56:59], v[48:51], v[16:31]
	s_waitcnt lgkmcnt(2)
	v_mfma_f32_32x32x16_bf16 v[32:47], v[96:99], v[48:51], v[32:47]
	v_mfma_f32_32x32x16_bf16 v[16:31], v[60:63], v[52:55], v[16:31]
	s_waitcnt lgkmcnt(0)
	v_mfma_f32_32x32x16_bf16 v[32:47], v[128:131], v[52:55], v[32:47]
	v_mov_b32_e32 v165, v164
	s_nop 8
	v_mul_f32_e64 v18, v164, v18
	v_mul_f32_e64 v19, v165, v19
	v_mul_f32_e64 v16, v166, v16
	v_mul_f32_e64 v17, v167, v17
	v_pk_mul_f32 v[22:23], v[164:165], v[22:23]
	v_cvt_pk_bf16_f32 v14, v16, v17
	v_cvt_pk_bf16_f32 v15, v18, v19
	v_pk_mul_f32 v[20:21], v[164:165], v[20:21]
	v_pk_mul_f32 v[34:35], v[164:165], v[34:35]
	v_pk_mul_f32 v[32:33], v[166:167], v[32:33]
	s_add_u32 s84, s84, 0x100000
	v_cvt_pk_bf16_f32 v48, v32, v33
	v_cvt_pk_bf16_f32 v49, v34, v35
	ds_write_b64 v185, v[14:15]
	ds_write_b64 v186, v[48:49]
	v_cvt_pk_bf16_f32 v14, v20, v21
	v_cvt_pk_bf16_f32 v15, v22, v23
	v_pk_mul_f32 v[26:27], v[164:165], v[26:27]
	v_pk_mul_f32 v[24:25], v[164:165], v[24:25]
	v_pk_mul_f32 v[38:39], v[164:165], v[38:39]
	v_pk_mul_f32 v[36:37], v[164:165], v[36:37]
	s_addc_u32 s85, s85, 0
	v_cvt_pk_bf16_f32 v48, v36, v37
	v_cvt_pk_bf16_f32 v49, v38, v39
	ds_write_b64 v187, v[14:15]
	ds_write_b64 v188, v[48:49]
	v_cvt_pk_bf16_f32 v14, v24, v25
	v_cvt_pk_bf16_f32 v15, v26, v27
	s_waitcnt vmcnt(2)
	v_mov_b64_e32 v[98:99], v[78:79]
	v_mov_b64_e32 v[130:131], v[74:75]
	v_pk_mul_f32 v[30:31], v[164:165], v[30:31]
	v_pk_mul_f32 v[28:29], v[164:165], v[28:29]
	v_pk_mul_f32 v[46:47], v[164:165], v[46:47]
	v_pk_mul_f32 v[44:45], v[164:165], v[44:45]
	v_pk_mul_f32 v[42:43], v[164:165], v[42:43]
	v_pk_mul_f32 v[40:41], v[164:165], v[40:41]
	s_cmp_eq_u32 s84, 0x2100000
	v_cvt_pk_bf16_f32 v48, v40, v41
	v_cvt_pk_bf16_f32 v49, v42, v43
	ds_write_b64 v189, v[14:15]
	ds_write_b64 v190, v[48:49]
	v_cvt_pk_bf16_f32 v14, v28, v29
	v_cvt_pk_bf16_f32 v15, v30, v31
	s_mov_b64 s[76:77], s[56:57]
	v_mov_b64_e32 v[96:97], v[76:77]
	v_mov_b64_e32 v[128:129], v[72:73]
	v_cvt_pk_bf16_f32 v48, v44, v45
	v_cvt_pk_bf16_f32 v49, v46, v47
	ds_write_b64 v191, v[14:15]
	ds_write_b64 v192, v[48:49]
	s_cbranch_scc1 .LBB0_261
